# mLSTM state update: k slots of each 8-token group taken in order 0,2,4,6,1,3,5,7 in K^T, ws*V and ws operands so the transposed LDS reads are bank-conflict free
# speedup vs baseline: 1.0028x; 1.0028x over previous
.LBB0_734:
	s_or_b64 exec, exec, s[80:81]
	v_cndmask_b32_e64 v171, v79, v87, s[62:63]
	v_cndmask_b32_e64 v170, v78, v86, s[62:63]
	v_cndmask_b32_e64 v169, v77, v85, s[62:63]
	v_cndmask_b32_e64 v168, v76, v84, s[62:63]
	v_cndmask_b32_e64 v172, v80, v88, s[62:63]
	v_add_u32_e32 v0, s11, v131
	v_cndmask_b32_e64 v175, v83, v91, s[62:63]
	v_cndmask_b32_e64 v174, v82, v90, s[62:63]
	v_cndmask_b32_e64 v173, v81, v89, s[62:63]
	ds_write_b128 v0, v[168:171]
	ds_write_b128 v0, v[172:175] offset:1024
	v_cndmask_b32_e64 v172, v84, v76, s[62:63]
	v_add_u32_e32 v76, s21, v131
	s_waitcnt lgkmcnt(0)
	s_barrier
	v_cndmask_b32_e64 v0, v87, v79, s[62:63]
	v_cndmask_b32_e64 v3, v86, v78, s[62:63]
	v_cndmask_b32_e64 v178, v85, v77, s[62:63]
	v_cndmask_b32_e64 v179, v91, v83, s[62:63]
	v_cndmask_b32_e64 v180, v90, v82, s[62:63]
	v_cndmask_b32_e64 v181, v89, v81, s[62:63]
	v_cndmask_b32_e64 v182, v88, v80, s[62:63]
	ds_read_b128 v[80:83], v76
	ds_read_b128 v[76:79], v76 offset:1024
	ds_read_b128 v[84:87], v159
	ds_read_b128 v[88:91], v160
	ds_read_b128 v[168:171], v161
	s_waitcnt lgkmcnt(4)
	v_add_f32_e32 v80, v172, v80
	v_lshl_add_u64 v[174:175], v[104:105], 0, s[88:89]
	s_waitcnt lgkmcnt(2)
	v_fma_f32 v80, v80, v84, v92
	s_waitcnt lgkmcnt(1)
	v_max_f32_e64 v88, |v88|, |v88|
	s_waitcnt lgkmcnt(0)
	v_max_f32_e32 v84, v168, v168
	v_max_f32_e32 v84, v88, v84
	v_div_scale_f32 v88, s[80:81], v84, v84, v80
	v_rcp_f32_e32 v92, v88
	s_mov_b32 s80, 0x3a800000
	v_add_f32_e32 v3, v3, v82
	v_fma_f32 v3, v3, v86, v94
	v_fma_f32 v168, -v88, v92, 1.0
	v_fmac_f32_e32 v92, v168, v92
	v_div_scale_f32 v168, vcc, v80, v84, v80
	v_mul_f32_e32 v172, v168, v92
	v_fma_f32 v173, -v88, v172, v168
	v_fmac_f32_e32 v172, v173, v92
	v_fma_f32 v88, -v88, v172, v168
	v_div_fmas_f32 v88, v88, v92, v172
	v_div_fixup_f32 v80, v88, v84, v80
	v_add_co_u32_e32 v176, vcc, s80, v174
	v_cvt_pk_bf16_f32 v80, v80, v1
	v_max_f32_e64 v84, |v89|, |v89|
	s_nop 0
	v_addc_co_u32_e32 v177, vcc, 0, v175, vcc
	global_store_short v[176:177], v80, off
	v_add_f32_e32 v80, v178, v81
	v_max_f32_e32 v81, v169, v169
	v_fma_f32 v80, v80, v85, v93
	v_max_f32_e32 v81, v84, v81
	v_div_scale_f32 v84, s[80:81], v81, v81, v80
	v_rcp_f32_e32 v85, v84
	v_lshl_add_u64 v[172:173], v[106:107], 0, s[88:89]
	v_add_f32_e32 v0, v0, v83
	v_fmac_f32_e32 v95, v0, v87
	v_fma_f32 v88, -v84, v85, 1.0
	v_fmac_f32_e32 v85, v88, v85
	v_div_scale_f32 v88, vcc, v80, v81, v80
	v_mul_f32_e32 v89, v88, v85
	v_fma_f32 v92, -v84, v89, v88
	v_fmac_f32_e32 v89, v92, v85
	v_fma_f32 v84, -v84, v89, v88
	v_div_fmas_f32 v84, v84, v85, v89
	v_div_fixup_f32 v80, v84, v81, v80
	v_cvt_pk_bf16_f32 v84, v80, v1
	v_or_b32_e32 v80, 0x800, v172
	v_mov_b32_e32 v81, v173
	v_lshl_add_u64 v[80:81], v[102:103], 0, v[80:81]
	global_store_short v[80:81], v84, off
	v_max_f32_e32 v80, v170, v170
	v_max_f32_e64 v81, |v90|, |v90|
	v_max_f32_e32 v80, v81, v80
	v_div_scale_f32 v81, s[80:81], v80, v80, v3
	v_rcp_f32_e32 v82, v81
	v_max_f32_e32 v0, v171, v171
	v_lshl_add_u64 v[92:93], v[172:173], 0, s[96:97]
	v_fma_f32 v84, -v81, v82, 1.0
	v_fmac_f32_e32 v82, v84, v82
	v_div_scale_f32 v84, vcc, v3, v80, v3
	v_mul_f32_e32 v85, v84, v82
	v_fma_f32 v86, -v81, v85, v84
	v_fmac_f32_e32 v85, v86, v82
	v_fma_f32 v81, -v81, v85, v84
	v_div_fmas_f32 v81, v81, v82, v85
	v_div_fixup_f32 v3, v81, v80, v3
	v_or_b32_e32 v80, 0x1000, v172
	v_mov_b32_e32 v81, v173
	v_cvt_pk_bf16_f32 v3, v3, v1
	v_lshl_add_u64 v[80:81], v[102:103], 0, v[80:81]
	global_store_short v[80:81], v3, off
	v_max_f32_e64 v3, |v91|, |v91|
	v_max_f32_e32 v0, v3, v0
	v_div_scale_f32 v3, s[80:81], v0, v0, v95
	v_rcp_f32_e32 v80, v3
	s_nop 0
	v_fma_f32 v81, -v3, v80, 1.0
	v_fmac_f32_e32 v80, v81, v80
	v_div_scale_f32 v81, vcc, v95, v0, v95
	v_mul_f32_e32 v82, v81, v80
	v_fma_f32 v83, -v3, v82, v81
	v_fmac_f32_e32 v82, v83, v80
	v_fma_f32 v3, -v3, v82, v81
	v_div_fmas_f32 v3, v3, v80, v82
	v_or_b32_e32 v80, 0x1800, v172
	v_mov_b32_e32 v81, v173
	v_div_fixup_f32 v0, v3, v0, v95
	v_lshl_add_u64 v[80:81], v[102:103], 0, v[80:81]
	v_cvt_pk_bf16_f32 v0, v0, v1
	global_store_short v[80:81], v0, off
	ds_read_b128 v[80:83], v159 offset:64
	ds_read_b128 v[84:87], v160 offset:64
	ds_read_b128 v[88:91], v161 offset:64
	v_add_f32_e32 v0, v182, v76
	s_waitcnt lgkmcnt(0)
	v_fma_f32 v0, v0, v80, v72
	v_max_f32_e64 v72, |v84|, |v84|
	v_max_f32_e32 v3, v88, v88
	v_max_f32_e32 v3, v72, v3
	v_div_scale_f32 v72, s[80:81], v3, v3, v0
	v_rcp_f32_e32 v76, v72
	s_mov_b32 s80, 0x3a808000
	v_fma_f32 v80, -v72, v76, 1.0
	v_fmac_f32_e32 v76, v80, v76
	v_div_scale_f32 v80, vcc, v0, v3, v0
	v_mul_f32_e32 v84, v80, v76
	v_fma_f32 v88, -v72, v84, v80
	v_fmac_f32_e32 v84, v88, v76
	v_fma_f32 v72, -v72, v84, v80
	v_div_fmas_f32 v72, v72, v76, v84
	v_div_fixup_f32 v0, v72, v3, v0
	v_add_co_u32_e32 v94, vcc, s80, v174
	v_cvt_pk_bf16_f32 v0, v0, v1
	v_max_f32_e32 v3, v89, v89
	s_nop 0
	v_addc_co_u32_e32 v95, vcc, 0, v175, vcc
	global_store_short v[94:95], v0, off
	v_add_f32_e32 v0, v181, v77
	v_max_f32_e64 v72, |v85|, |v85|
	v_fma_f32 v0, v0, v81, v73
	v_max_f32_e32 v3, v72, v3
	v_div_scale_f32 v72, s[80:81], v3, v3, v0
	v_rcp_f32_e32 v73, v72
	v_add_u32_e32 v94, 0, v2
	v_fma_f32 v76, -v72, v73, 1.0
	v_fmac_f32_e32 v73, v76, v73
	v_div_scale_f32 v76, vcc, v0, v3, v0
	v_mul_f32_e32 v77, v76, v73
	v_fma_f32 v80, -v72, v77, v76
	v_fmac_f32_e32 v77, v80, v73
	v_fma_f32 v72, -v72, v77, v76
	v_div_fmas_f32 v72, v72, v73, v77
	v_div_fixup_f32 v0, v72, v3, v0
	v_or_b32_e32 v72, 0x800, v92
	v_mov_b32_e32 v73, v93
	v_cvt_pk_bf16_f32 v0, v0, v1
	v_lshl_add_u64 v[72:73], v[102:103], 0, v[72:73]
	global_store_short v[72:73], v0, off
	v_add_f32_e32 v0, v180, v78
	v_max_f32_e32 v3, v90, v90
	v_max_f32_e64 v72, |v86|, |v86|
	v_fma_f32 v0, v0, v82, v74
	v_max_f32_e32 v3, v72, v3
	v_div_scale_f32 v72, s[80:81], v3, v3, v0
	v_rcp_f32_e32 v73, v72
	s_nop 0
	v_fma_f32 v74, -v72, v73, 1.0
	v_fmac_f32_e32 v73, v74, v73
	v_div_scale_f32 v74, vcc, v0, v3, v0
	v_mul_f32_e32 v76, v74, v73
	v_fma_f32 v77, -v72, v76, v74
	v_fmac_f32_e32 v76, v77, v73
	v_fma_f32 v72, -v72, v76, v74
	v_div_fmas_f32 v72, v72, v73, v76
	v_div_fixup_f32 v0, v72, v3, v0
	v_or_b32_e32 v72, 0x1000, v92
	v_mov_b32_e32 v73, v93
	v_cvt_pk_bf16_f32 v0, v0, v1
	v_lshl_add_u64 v[72:73], v[102:103], 0, v[72:73]
	global_store_short v[72:73], v0, off
	v_add_f32_e32 v0, v179, v79
	v_fmac_f32_e32 v75, v0, v83
	v_max_f32_e32 v0, v91, v91
	v_max_f32_e64 v3, |v87|, |v87|
	v_max_f32_e32 v0, v3, v0
	v_div_scale_f32 v3, s[80:81], v0, v0, v75
	v_rcp_f32_e32 v72, v3
	v_or_b32_e32 v92, 0x1800, v92
	v_fma_f32 v73, -v3, v72, 1.0
	v_fmac_f32_e32 v72, v73, v72
	v_div_scale_f32 v73, vcc, v75, v0, v75
	v_mul_f32_e32 v74, v73, v72
	v_fma_f32 v76, -v3, v74, v73
	v_fmac_f32_e32 v74, v76, v72
	v_fma_f32 v3, -v3, v74, v73
	v_div_fmas_f32 v3, v3, v72, v74
	v_div_fixup_f32 v0, v3, v0, v75
	v_cvt_pk_bf16_f32 v0, v0, v1
	v_lshl_add_u64 v[72:73], v[102:103], 0, v[92:93]
	global_store_short v[72:73], v0, off
	v_mov_b32_e32 v0, s19
	ds_read_b32 v92, v0
	v_bfe_u32 v89, v110, 4, 2
	v_mul_u32_u24_e32 v0, 0x90, v89
	v_add_u32_e32 v0, v0, v167
	v_add_u32_e32 v3, 0x13e00, v0
	v_add_u32_e32 v0, 0x12c00, v0
	ds_read_b64_tr_b16 v[80:81], v0
	ds_read_b64_tr_b16 v[82:83], v0 offset:144
	ds_read_b128 v[72:75], v135
	ds_read_b128 v[76:79], v135 offset:16
	ds_read_b64_tr_b16 v[206:207], v3
	ds_read_b64_tr_b16 v[208:209], v3 offset:144
	v_mul_u32_u24_e32 v89, 0x210, v89
	v_add_u32_e32 v90, v89, v94
	ds_read_b128 v[198:201], v135 offset:128
	ds_read_b128 v[202:205], v135 offset:144
	s_mov_b32 s98, 0
	s_and_b64 vcc, exec, s[28:29]
	s_cselect_b32 s98, 64, s98
	s_and_b64 vcc, exec, s[30:31]
	s_cselect_b32 s98, 0x80, s98
	s_and_b64 vcc, exec, s[34:35]
	s_cselect_b32 s98, 0xc0, s98
	v_add_u32_e32 v88, s98, v90
	ds_read_b64_tr_b16 v[168:169], v90
	ds_read_b64_tr_b16 v[170:171], v90 offset:528
	ds_read_b64_tr_b16 v[172:173], v90 offset:32
	ds_read_b64_tr_b16 v[174:175], v90 offset:560
	ds_read_b64_tr_b16 v[176:177], v90 offset:64
	ds_read_b64_tr_b16 v[178:179], v90 offset:592
	s_waitcnt lgkmcnt(6)
	v_cvt_pk_bf16_f32 v84, v72, v74
	v_cvt_pk_bf16_f32 v85, v76, v78
	v_cvt_pk_bf16_f32 v86, v73, v75
	v_cvt_pk_bf16_f32 v87, v77, v79
	v_cvt_pk_bf16_f32 v194, v198, v200
	v_cvt_pk_bf16_f32 v195, v202, v204
	v_cvt_pk_bf16_f32 v196, v199, v201
	v_cvt_pk_bf16_f32 v197, v203, v205
	v_mov_b32_e32 v93, v92
	v_pk_mul_f32 v[68:69], v[68:69], v[92:93]
	v_pk_mul_f32 v[70:71], v[70:71], v[92:93]
	v_pk_mul_f32 v[64:65], v[64:65], v[92:93]
	v_pk_mul_f32 v[66:67], v[66:67], v[92:93]
	v_pk_mul_f32 v[56:57], v[56:57], v[92:93]
	v_pk_mul_f32 v[58:59], v[58:59], v[92:93]
	v_pk_mul_f32 v[60:61], v[60:61], v[92:93]
	v_pk_mul_f32 v[62:63], v[62:63], v[92:93]
	v_pk_mul_f32 v[48:49], v[48:49], v[92:93]
	v_pk_mul_f32 v[50:51], v[50:51], v[92:93]
	v_pk_mul_f32 v[52:53], v[52:53], v[92:93]
	v_pk_mul_f32 v[54:55], v[54:55], v[92:93]
	v_pk_mul_f32 v[40:41], v[40:41], v[92:93]
	v_pk_mul_f32 v[42:43], v[42:43], v[92:93]
	v_pk_mul_f32 v[44:45], v[44:45], v[92:93]
	v_pk_mul_f32 v[46:47], v[46:47], v[92:93]
	ds_read_b64_tr_b16 v[180:181], v90 offset:96
	ds_read_b64_tr_b16 v[182:183], v90 offset:624
	ds_read_b64_tr_b16 v[184:185], v90 offset:128
	ds_read_b64_tr_b16 v[186:187], v90 offset:656
	ds_read_b64_tr_b16 v[188:189], v90 offset:160
	ds_read_b64_tr_b16 v[190:191], v90 offset:688
	s_waitcnt lgkmcnt(10)
	v_mfma_f32_16x16x32_bf16 v[68:71], v[168:171], v[80:83], v[68:71]
	ds_read_b64_tr_b16 v[168:169], v90 offset:192
	ds_read_b64_tr_b16 v[170:171], v90 offset:720
	s_waitcnt lgkmcnt(10)
	v_mfma_f32_16x16x32_bf16 v[64:67], v[172:175], v[80:83], v[64:67]
	ds_read_b64_tr_b16 v[172:173], v90 offset:224
	ds_read_b64_tr_b16 v[174:175], v90 offset:752
	s_waitcnt lgkmcnt(10)
	v_mfma_f32_16x16x32_bf16 v[56:59], v[176:179], v[80:83], v[56:59]
	ds_read_b64_tr_b16 v[176:177], v88
	ds_read_b64_tr_b16 v[178:179], v88 offset:528
	s_waitcnt lgkmcnt(10)
	v_mfma_f32_16x16x32_bf16 v[60:63], v[180:183], v[80:83], v[60:63]
	ds_read_b64_tr_b16 v[180:181], v88 offset:32
	ds_read_b64_tr_b16 v[182:183], v88 offset:560
	s_waitcnt lgkmcnt(10)
	v_mfma_f32_16x16x32_bf16 v[48:51], v[184:187], v[80:83], v[48:51]
	ds_read_b64_tr_b16 v[184:185], v90 offset:16896
	ds_read_b64_tr_b16 v[186:187], v90 offset:17424
	s_waitcnt lgkmcnt(10)
	v_mfma_f32_16x16x32_bf16 v[52:55], v[188:191], v[80:83], v[52:55]
	ds_read_b64_tr_b16 v[188:189], v90 offset:16928
	ds_read_b64_tr_b16 v[190:191], v90 offset:17456
	s_waitcnt lgkmcnt(10)
	v_mfma_f32_16x16x32_bf16 v[40:43], v[168:171], v[80:83], v[40:43]
	ds_read_b64_tr_b16 v[168:169], v90 offset:16960
	ds_read_b64_tr_b16 v[170:171], v90 offset:17488
	s_waitcnt lgkmcnt(10)
	v_mfma_f32_16x16x32_bf16 v[44:47], v[172:175], v[80:83], v[44:47]
	ds_read_b64_tr_b16 v[172:173], v90 offset:16992
	ds_read_b64_tr_b16 v[174:175], v90 offset:17520
	s_waitcnt lgkmcnt(10)
	v_mfma_f32_16x16x32_bf16 v[72:75], v[176:179], v[84:87], 0
	ds_read_b64_tr_b16 v[176:177], v90 offset:17024
	ds_read_b64_tr_b16 v[178:179], v90 offset:17552
	s_waitcnt lgkmcnt(10)
	v_mfma_f32_16x16x32_bf16 v[76:79], v[180:183], v[84:87], 0
	ds_read_b64_tr_b16 v[180:181], v90 offset:17056
	ds_read_b64_tr_b16 v[182:183], v90 offset:17584
	s_waitcnt lgkmcnt(10)
	v_mfma_f32_16x16x32_bf16 v[68:71], v[184:187], v[206:209], v[68:71]
	ds_read_b64_tr_b16 v[184:185], v90 offset:17088
	ds_read_b64_tr_b16 v[186:187], v90 offset:17616
	s_waitcnt lgkmcnt(10)
	v_mfma_f32_16x16x32_bf16 v[64:67], v[188:191], v[206:209], v[64:67]
	ds_read_b64_tr_b16 v[188:189], v90 offset:17120
	ds_read_b64_tr_b16 v[190:191], v90 offset:17648
	s_waitcnt lgkmcnt(10)
	v_mfma_f32_16x16x32_bf16 v[56:59], v[168:171], v[206:209], v[56:59]
	ds_read_b64_tr_b16 v[168:169], v88 offset:16896
	ds_read_b64_tr_b16 v[170:171], v88 offset:17424
	s_waitcnt lgkmcnt(10)
	v_mfma_f32_16x16x32_bf16 v[60:63], v[172:175], v[206:209], v[60:63]
	ds_read_b64_tr_b16 v[172:173], v88 offset:16928
	ds_read_b64_tr_b16 v[174:175], v88 offset:17456
	s_waitcnt lgkmcnt(10)
	v_mfma_f32_16x16x32_bf16 v[48:51], v[176:179], v[206:209], v[48:51]
	s_waitcnt lgkmcnt(8)
	v_mfma_f32_16x16x32_bf16 v[52:55], v[180:183], v[206:209], v[52:55]
	s_waitcnt lgkmcnt(6)
	v_mfma_f32_16x16x32_bf16 v[40:43], v[184:187], v[206:209], v[40:43]
	s_waitcnt lgkmcnt(4)
	v_mfma_f32_16x16x32_bf16 v[44:47], v[188:191], v[206:209], v[44:47]
	s_waitcnt lgkmcnt(2)
	v_mfma_f32_16x16x32_bf16 v[72:75], v[168:171], v[194:197], v[72:75]
	s_waitcnt lgkmcnt(0)
	v_mfma_f32_16x16x32_bf16 v[76:79], v[172:175], v[194:197], v[76:79]
	s_mov_b32 s99, 64
	s_and_b64 vcc, exec, s[62:63]
	s_cselect_b32 s99, 0, s99
	s_or_b64 vcc, s[30:31], s[34:35]
	s_and_b64 vcc, exec, vcc
	s_cselect_b32 s98, 32, 0
	s_or_b32 s99, s99, s98
	s_and_saveexec_b64 s[80:81], s[60:61]
	s_cbranch_execz .LBB0_725
	v_xor_b32_e32 v88, s99, v154
	v_add_u32_e32 v89, 64, v154
	v_xor_b32_e32 v89, s99, v89
	ds_read_b128 v[80:83], v88
	ds_read_b128 v[84:87], v89
	s_nop 7
	s_waitcnt lgkmcnt(1)
	v_pk_fma_f32 v[74:75], v[92:93], v[82:83], v[74:75]
	v_pk_fma_f32 v[72:73], v[92:93], v[80:81], v[72:73]
	s_waitcnt lgkmcnt(0)
	v_pk_fma_f32 v[78:79], v[92:93], v[86:87], v[78:79]
	v_pk_fma_f32 v[76:77], v[92:93], v[84:85], v[76:77]
	ds_write_b128 v88, v[72:75]
	ds_write_b128 v89, v[76:79]
	s_branch .LBB0_725
